# speedup vs baseline: 1.0191x; 1.0150x over previous
_Z9fast_mainILb0EEvPKiS1_S1_PKfPKcS3_PfS6_PiPyS6_:
	s_nop 0
	s_nop 0
	s_nop 0
	s_nop 0
	s_nop 0
	s_nop 0
	s_nop 0
	s_nop 0
	s_nop 0
	s_nop 0
	s_nop 0
	s_nop 0
	s_nop 0
	s_nop 0
	s_nop 0
	s_nop 0
	s_load_dwordx4 s[4:7], s[0:1], 0x20
	s_load_dwordx4 s[8:11], s[0:1], 0x8
	s_load_dwordx2 s[16:17], s[0:1], 0x0
	v_and_b32_e32 v1, 63, v0
	v_lshrrev_b32_e32 v8, 6, v0
	v_lshlrev_b32_e32 v150, 4, v1
	v_lshl_or_b32 v14, s2, 3, v8
	v_lshlrev_b32_e32 v14, 10, v14
	v_or_b32_e32 v14, v14, v150
	v_add_u32_e32 v212, 0x10000, v150
	v_add_u32_e32 v213, 0x18c00, v150
	v_mov_b32_e32 v151, 0
	s_waitcnt lgkmcnt(0)
	global_load_dwordx4 v[20:23], v14, s[16:17]
	v_lshl_add_u64 v[4:5], s[4:5], 0, v[150:151]
	v_lshlrev_b32_e32 v2, 10, v8
	v_mov_b32_e32 v3, v151
	v_lshl_add_u64 v[6:7], v[4:5], 0, v[2:3]
	v_readfirstlane_b32 s3, v2
	v_or_b32_e32 v3, 0x2000, v2
	s_mov_b32 m0, s3
	s_mov_b64 s[4:5], 0x2000
	v_readfirstlane_b32 s3, v3
	global_load_lds_dwordx4 v[6:7], off
	v_lshl_add_u64 v[10:11], v[6:7], 0, s[4:5]
	s_mov_b32 m0, s3
	v_or_b32_e32 v3, 0x6000, v2
	global_load_lds_dwordx4 v[10:11], off
	v_or_b32_e32 v10, 0x4000, v2
	v_mov_b32_e32 v11, v151
	v_readfirstlane_b32 s3, v10
	v_lshl_add_u64 v[12:13], v[4:5], 0, v[10:11]
	s_mov_b32 m0, s3
	s_mov_b64 s[4:5], 0x6000
	v_readfirstlane_b32 s3, v3
	global_load_lds_dwordx4 v[12:13], off
	v_lshl_add_u64 v[10:11], v[6:7], 0, s[4:5]
	s_mov_b32 m0, s3
	v_or_b32_e32 v3, 0xa000, v2
	global_load_lds_dwordx4 v[10:11], off
	v_or_b32_e32 v10, 0x8000, v2
	v_mov_b32_e32 v11, v151
	v_readfirstlane_b32 s3, v10
	v_lshl_add_u64 v[12:13], v[4:5], 0, v[10:11]
	s_mov_b32 m0, s3
	s_mov_b64 s[4:5], 0xa000
	v_readfirstlane_b32 s3, v3
	global_load_lds_dwordx4 v[12:13], off
	v_lshl_add_u64 v[10:11], v[6:7], 0, s[4:5]
	s_mov_b32 m0, s3
	v_or_b32_e32 v3, 0xe000, v2
	global_load_lds_dwordx4 v[10:11], off
	v_or_b32_e32 v10, 0xc000, v2
	v_mov_b32_e32 v11, v151
	v_readfirstlane_b32 s3, v10
	v_lshl_add_u64 v[12:13], v[4:5], 0, v[10:11]
	s_mov_b32 m0, s3
	s_mov_b64 s[4:5], 0xe000
	v_readfirstlane_b32 s3, v3
	global_load_lds_dwordx4 v[12:13], off
	v_lshl_add_u64 v[10:11], v[6:7], 0, s[4:5]
	s_mov_b32 m0, s3
	v_or_b32_e32 v3, 0x12000, v2
	global_load_lds_dwordx4 v[10:11], off
	v_or_b32_e32 v10, 0x10000, v2
	v_mov_b32_e32 v11, v151
	v_readfirstlane_b32 s3, v10
	v_lshl_add_u64 v[12:13], v[4:5], 0, v[10:11]
	s_mov_b32 m0, s3
	s_mov_b64 s[4:5], 0x12000
	v_readfirstlane_b32 s3, v3
	global_load_lds_dwordx4 v[12:13], off
	v_lshl_add_u64 v[10:11], v[6:7], 0, s[4:5]
	s_mov_b32 m0, s3
	s_nop 0
	global_load_lds_dwordx4 v[10:11], off
	v_or_b32_e32 v10, 0x14000, v2
	v_mov_b32_e32 v11, v151
	v_readfirstlane_b32 s3, v10
	v_lshl_add_u64 v[12:13], v[4:5], 0, v[10:11]
	s_mov_b32 m0, s3
	s_movk_i32 s3, 0x2c0
	global_load_lds_dwordx4 v[12:13], off
	v_cmp_gt_u32_e32 vcc, s3, v0
	s_and_saveexec_b64 s[4:5], vcc
	s_cbranch_execz .LBB1_2
	v_or_b32_e32 v3, 0x16000, v2
	s_mov_b64 s[12:13], 0x16000
	v_readfirstlane_b32 s3, v3
	v_lshl_add_u64 v[6:7], v[6:7], 0, s[12:13]
	s_mov_b32 m0, s3
	s_nop 0
	global_load_lds_dwordx4 v[6:7], off
